# in-place rope of k_slc/k_win: 8 serialized load-rotate-store trips turned into one batch of 32 loads then rotate+store
# baseline (speedup 1.0000x reference)
; __device__ __forceinline__ unsigned f2bf(float f) { unsigned u = __builtin_bit_cast(unsigned, f); return (u + 0x7fffu + ((u >> 16) & 1u)) >> 16; }
; template <int L, bool WITH_LA> __device__ __forceinline__ void p_rope_la(const Args& a) {
;     bf16* proj = (bf16*)(a.ws + WS_PROJ);
;     const float* rope = (const float*)(a.ws + WS_ROPE);
;     const int gt = blockIdx.x * 512 + threadIdx.x, NGT = gridDim.x * 512;
;     for (int idx = gt; idx < M * 64; idx += NGT) {
;         const int i = idx & 15, hh = (idx >> 4) & 1, ts = (idx >> 5) & 1, m = idx >> 6, t = m & (T - 1);
;         bf16* p = proj + (size_t)m * PW + (ts ? PKW : PKS) + hh * 128 + i;
;         const float x1 = bf1(p[0]), x2 = bf1(p[16]), c = rope[t * 32 + i], s = rope[t * 32 + 16 + i];
;         p[0] = (bf16)f2bf(x1 * c - x2 * s); p[16] = (bf16)f2bf(x2 * c + x1 * s);
;     }
.LBB0_563:
	v_readlane_b32 s0, v255, 0
	s_waitcnt vmcnt(0)
	s_nop 0
	v_lshl_or_b32 v3, s0, 9, v0
	s_mov_b32 s0, 0x100000
	v_cmp_gt_i32_e32 vcc, s0, v3
	s_and_saveexec_b64 s[0:1], vcc
	s_cbranch_execz .LBB0_566
	s_add_u32 s2, s66, 0x200000
	v_and_b32_e32 v2, 15, v0
	v_mov_b32_e32 v5, 0
	v_lshlrev_b32_e32 v4, 3, v0
	v_readlane_b32 s4, v255, 0
	s_addc_u32 s3, s67, 0
	s_waitcnt lgkmcnt(0)
	s_lshl_b32 s6, s42, 9
	v_lshl_or_b32 v10, s4, 12, v4
	s_lshl_b32 s7, s42, 12
	s_mov_b64 s[4:5], 0
	s_movk_i32 s8, 0x2e00
	v_mov_b64_e32 v[6:7], s[18:19]
	v_mov_b32_e32 v11, 0x1000
	v_mov_b32_e32 v12, 0xc00
	v_lshlrev_b32_e32 v8, 1, v2
	v_mov_b32_e32 v9, v5
	s_mov_b32 s9, 0x1ffe0
	s_movk_i32 s10, 0x7fff
	s_mov_b32 s11, 0xfffff
	s_cmpk_lg_u32 s42, 0x100
	s_cbranch_scc1 .LBB0_565
	v_and_b32_e32 v4, 32, v3
	v_ashrrev_i32_e32 v13, 6, v3
	v_cmp_eq_u32_e32 vcc, 0, v4
	v_and_b32_e32 v16, 0x80, v10
	v_mad_i64_i32 v[190:191], s[12:13], v13, s8, v[6:7]
	v_cndmask_b32_e32 v4, v11, v12, vcc
	v_lshlrev_b32_e32 v13, 5, v13
	v_lshl_add_u64 v[190:191], v[190:191], 0, v[4:5]
	v_lshlrev_b32_e32 v4, 1, v16
	v_and_or_b32 v13, v13, s9, v2
	v_lshl_add_u64 v[190:191], v[190:191], 0, v[4:5]
	v_lshlrev_b32_e32 v4, 2, v13
	v_lshl_add_u64 v[190:191], v[190:191], 0, v[8:9]
	global_load_ushort v206, v[190:191], off
	global_load_ushort v207, v[190:191], off offset:32
	global_load_dword v208, v4, s[2:3] offset:64
	s_nop 0
	global_load_dword v209, v4, s[2:3]
	v_add_u32_e32 v3, s6, v3
	v_add_u32_e32 v10, s7, v10
	v_and_b32_e32 v4, 32, v3
	v_ashrrev_i32_e32 v13, 6, v3
	v_cmp_eq_u32_e32 vcc, 0, v4
	v_and_b32_e32 v16, 0x80, v10
	v_mad_i64_i32 v[192:193], s[12:13], v13, s8, v[6:7]
	v_cndmask_b32_e32 v4, v11, v12, vcc
	v_lshlrev_b32_e32 v13, 5, v13
	v_lshl_add_u64 v[192:193], v[192:193], 0, v[4:5]
	v_lshlrev_b32_e32 v4, 1, v16
	v_and_or_b32 v13, v13, s9, v2
	v_lshl_add_u64 v[192:193], v[192:193], 0, v[4:5]
	v_lshlrev_b32_e32 v4, 2, v13
	v_lshl_add_u64 v[192:193], v[192:193], 0, v[8:9]
	global_load_ushort v210, v[192:193], off
	global_load_ushort v211, v[192:193], off offset:32
	global_load_dword v212, v4, s[2:3] offset:64
	s_nop 0
	global_load_dword v213, v4, s[2:3]
	v_add_u32_e32 v3, s6, v3
	v_add_u32_e32 v10, s7, v10
	v_and_b32_e32 v4, 32, v3
	v_ashrrev_i32_e32 v13, 6, v3
	v_cmp_eq_u32_e32 vcc, 0, v4
	v_and_b32_e32 v16, 0x80, v10
	v_mad_i64_i32 v[194:195], s[12:13], v13, s8, v[6:7]
	v_cndmask_b32_e32 v4, v11, v12, vcc
	v_lshlrev_b32_e32 v13, 5, v13
	v_lshl_add_u64 v[194:195], v[194:195], 0, v[4:5]
	v_lshlrev_b32_e32 v4, 1, v16
	v_and_or_b32 v13, v13, s9, v2
	v_lshl_add_u64 v[194:195], v[194:195], 0, v[4:5]
	v_lshlrev_b32_e32 v4, 2, v13
	v_lshl_add_u64 v[194:195], v[194:195], 0, v[8:9]
	global_load_ushort v214, v[194:195], off
	global_load_ushort v215, v[194:195], off offset:32
	global_load_dword v216, v4, s[2:3] offset:64
	s_nop 0
	global_load_dword v217, v4, s[2:3]
	v_add_u32_e32 v3, s6, v3
	v_add_u32_e32 v10, s7, v10
	v_and_b32_e32 v4, 32, v3
	v_ashrrev_i32_e32 v13, 6, v3
	v_cmp_eq_u32_e32 vcc, 0, v4
	v_and_b32_e32 v16, 0x80, v10
	v_mad_i64_i32 v[196:197], s[12:13], v13, s8, v[6:7]
	v_cndmask_b32_e32 v4, v11, v12, vcc
	v_lshlrev_b32_e32 v13, 5, v13
	v_lshl_add_u64 v[196:197], v[196:197], 0, v[4:5]
	v_lshlrev_b32_e32 v4, 1, v16
	v_and_or_b32 v13, v13, s9, v2
	v_lshl_add_u64 v[196:197], v[196:197], 0, v[4:5]
	v_lshlrev_b32_e32 v4, 2, v13
	v_lshl_add_u64 v[196:197], v[196:197], 0, v[8:9]
	global_load_ushort v218, v[196:197], off
	global_load_ushort v219, v[196:197], off offset:32
	global_load_dword v220, v4, s[2:3] offset:64
	s_nop 0
	global_load_dword v221, v4, s[2:3]
	v_add_u32_e32 v3, s6, v3
	v_add_u32_e32 v10, s7, v10
	v_and_b32_e32 v4, 32, v3
	v_ashrrev_i32_e32 v13, 6, v3
	v_cmp_eq_u32_e32 vcc, 0, v4
	v_and_b32_e32 v16, 0x80, v10
	v_mad_i64_i32 v[198:199], s[12:13], v13, s8, v[6:7]
	v_cndmask_b32_e32 v4, v11, v12, vcc
	v_lshlrev_b32_e32 v13, 5, v13
	v_lshl_add_u64 v[198:199], v[198:199], 0, v[4:5]
	v_lshlrev_b32_e32 v4, 1, v16
	v_and_or_b32 v13, v13, s9, v2
	v_lshl_add_u64 v[198:199], v[198:199], 0, v[4:5]
	v_lshlrev_b32_e32 v4, 2, v13
	v_lshl_add_u64 v[198:199], v[198:199], 0, v[8:9]
	global_load_ushort v222, v[198:199], off
	global_load_ushort v223, v[198:199], off offset:32
	global_load_dword v224, v4, s[2:3] offset:64
	s_nop 0
	global_load_dword v225, v4, s[2:3]
	v_add_u32_e32 v3, s6, v3
	v_add_u32_e32 v10, s7, v10
	v_and_b32_e32 v4, 32, v3
	v_ashrrev_i32_e32 v13, 6, v3
	v_cmp_eq_u32_e32 vcc, 0, v4
	v_and_b32_e32 v16, 0x80, v10
	v_mad_i64_i32 v[200:201], s[12:13], v13, s8, v[6:7]
	v_cndmask_b32_e32 v4, v11, v12, vcc
	v_lshlrev_b32_e32 v13, 5, v13
	v_lshl_add_u64 v[200:201], v[200:201], 0, v[4:5]
	v_lshlrev_b32_e32 v4, 1, v16
	v_and_or_b32 v13, v13, s9, v2
	v_lshl_add_u64 v[200:201], v[200:201], 0, v[4:5]
	v_lshlrev_b32_e32 v4, 2, v13
	v_lshl_add_u64 v[200:201], v[200:201], 0, v[8:9]
	global_load_ushort v226, v[200:201], off
	global_load_ushort v227, v[200:201], off offset:32
	global_load_dword v228, v4, s[2:3] offset:64
	s_nop 0
	global_load_dword v229, v4, s[2:3]
	v_add_u32_e32 v3, s6, v3
	v_add_u32_e32 v10, s7, v10
	v_and_b32_e32 v4, 32, v3
	v_ashrrev_i32_e32 v13, 6, v3
	v_cmp_eq_u32_e32 vcc, 0, v4
	v_and_b32_e32 v16, 0x80, v10
	v_mad_i64_i32 v[202:203], s[12:13], v13, s8, v[6:7]
	v_cndmask_b32_e32 v4, v11, v12, vcc
	v_lshlrev_b32_e32 v13, 5, v13
	v_lshl_add_u64 v[202:203], v[202:203], 0, v[4:5]
	v_lshlrev_b32_e32 v4, 1, v16
	v_and_or_b32 v13, v13, s9, v2
	v_lshl_add_u64 v[202:203], v[202:203], 0, v[4:5]
	v_lshlrev_b32_e32 v4, 2, v13
	v_lshl_add_u64 v[202:203], v[202:203], 0, v[8:9]
	global_load_ushort v230, v[202:203], off
	global_load_ushort v231, v[202:203], off offset:32
	global_load_dword v232, v4, s[2:3] offset:64
	s_nop 0
	global_load_dword v233, v4, s[2:3]
	v_add_u32_e32 v3, s6, v3
	v_add_u32_e32 v10, s7, v10
	v_and_b32_e32 v4, 32, v3
	v_ashrrev_i32_e32 v13, 6, v3
	v_cmp_eq_u32_e32 vcc, 0, v4
	v_and_b32_e32 v16, 0x80, v10
	v_mad_i64_i32 v[204:205], s[12:13], v13, s8, v[6:7]
	v_cndmask_b32_e32 v4, v11, v12, vcc
	v_lshlrev_b32_e32 v13, 5, v13
	v_lshl_add_u64 v[204:205], v[204:205], 0, v[4:5]
	v_lshlrev_b32_e32 v4, 1, v16
	v_and_or_b32 v13, v13, s9, v2
	v_lshl_add_u64 v[204:205], v[204:205], 0, v[4:5]
	v_lshlrev_b32_e32 v4, 2, v13
	v_lshl_add_u64 v[204:205], v[204:205], 0, v[8:9]
	global_load_ushort v234, v[204:205], off
	global_load_ushort v235, v[204:205], off offset:32
	global_load_dword v236, v4, s[2:3] offset:64
	s_nop 0
	global_load_dword v237, v4, s[2:3]
	v_add_u32_e32 v3, s6, v3
	v_add_u32_e32 v10, s7, v10
	s_waitcnt vmcnt(28)
; __device__ __forceinline__ unsigned f2bf(float f) { unsigned u = __builtin_bit_cast(unsigned, f); return (u + 0x7fffu + ((u >> 16) & 1u)) >> 16; }
; template <int L, bool WITH_LA> __device__ __forceinline__ void p_rope_la(const Args& a) {
;     ...
;     for (int idx = gt; idx < M * 64; idx += NGT) {
;         const int i = idx & 15, hh = (idx >> 4) & 1, ts = (idx >> 5) & 1, m = idx >> 6, t = m & (T - 1);
;         bf16* p = proj + (size_t)m * PW + (ts ? PKW : PKS) + hh * 128 + i;
;         const float x1 = bf1(p[0]), x2 = bf1(p[16]), c = rope[t * 32 + i], s = rope[t * 32 + 16 + i];
;         p[0] = (bf16)f2bf(x1 * c - x2 * s); p[16] = (bf16)f2bf(x2 * c + x1 * s);
;     }
	v_lshlrev_b32_e32 v206, 16, v206
	v_lshlrev_b32_e32 v207, 16, v207
	v_mul_f32_e32 v18, v208, v207
	v_mul_f32_e32 v207, v209, v207
	v_fma_f32 v209, v209, v206, -v18
	v_fmac_f32_e32 v207, v208, v206
	v_bfe_u32 v206, v209, 16, 1
	v_bfe_u32 v208, v207, 16, 1
	v_add3_u32 v209, v209, v206, s10
	v_add3_u32 v206, v207, v208, s10
	global_store_short_d16_hi v[190:191], v209, off
	global_store_short_d16_hi v[190:191], v206, off offset:32
	s_waitcnt vmcnt(26)
	v_lshlrev_b32_e32 v210, 16, v210
	v_lshlrev_b32_e32 v211, 16, v211
	v_mul_f32_e32 v18, v212, v211
	v_mul_f32_e32 v211, v213, v211
	v_fma_f32 v213, v213, v210, -v18
	v_fmac_f32_e32 v211, v212, v210
	v_bfe_u32 v210, v213, 16, 1
	v_bfe_u32 v212, v211, 16, 1
	v_add3_u32 v213, v213, v210, s10
	v_add3_u32 v210, v211, v212, s10
	global_store_short_d16_hi v[192:193], v213, off
	global_store_short_d16_hi v[192:193], v210, off offset:32
	s_waitcnt vmcnt(24)
	v_lshlrev_b32_e32 v214, 16, v214
	v_lshlrev_b32_e32 v215, 16, v215
	v_mul_f32_e32 v18, v216, v215
	v_mul_f32_e32 v215, v217, v215
	v_fma_f32 v217, v217, v214, -v18
	v_fmac_f32_e32 v215, v216, v214
	v_bfe_u32 v214, v217, 16, 1
	v_bfe_u32 v216, v215, 16, 1
	v_add3_u32 v217, v217, v214, s10
	v_add3_u32 v214, v215, v216, s10
	global_store_short_d16_hi v[194:195], v217, off
	global_store_short_d16_hi v[194:195], v214, off offset:32
	s_waitcnt vmcnt(22)
	v_lshlrev_b32_e32 v218, 16, v218
	v_lshlrev_b32_e32 v219, 16, v219
	v_mul_f32_e32 v18, v220, v219
	v_mul_f32_e32 v219, v221, v219
	v_fma_f32 v221, v221, v218, -v18
	v_fmac_f32_e32 v219, v220, v218
	v_bfe_u32 v218, v221, 16, 1
	v_bfe_u32 v220, v219, 16, 1
	v_add3_u32 v221, v221, v218, s10
	v_add3_u32 v218, v219, v220, s10
	global_store_short_d16_hi v[196:197], v221, off
	global_store_short_d16_hi v[196:197], v218, off offset:32
	s_waitcnt vmcnt(20)
	v_lshlrev_b32_e32 v222, 16, v222
	v_lshlrev_b32_e32 v223, 16, v223
	v_mul_f32_e32 v18, v224, v223
	v_mul_f32_e32 v223, v225, v223
	v_fma_f32 v225, v225, v222, -v18
	v_fmac_f32_e32 v223, v224, v222
	v_bfe_u32 v222, v225, 16, 1
	v_bfe_u32 v224, v223, 16, 1
	v_add3_u32 v225, v225, v222, s10
	v_add3_u32 v222, v223, v224, s10
	global_store_short_d16_hi v[198:199], v225, off
	global_store_short_d16_hi v[198:199], v222, off offset:32
	s_waitcnt vmcnt(18)
	v_lshlrev_b32_e32 v226, 16, v226
	v_lshlrev_b32_e32 v227, 16, v227
	v_mul_f32_e32 v18, v228, v227
	v_mul_f32_e32 v227, v229, v227
	v_fma_f32 v229, v229, v226, -v18
	v_fmac_f32_e32 v227, v228, v226
	v_bfe_u32 v226, v229, 16, 1
	v_bfe_u32 v228, v227, 16, 1
	v_add3_u32 v229, v229, v226, s10
	v_add3_u32 v226, v227, v228, s10
	global_store_short_d16_hi v[200:201], v229, off
	global_store_short_d16_hi v[200:201], v226, off offset:32
	s_waitcnt vmcnt(16)
	v_lshlrev_b32_e32 v230, 16, v230
	v_lshlrev_b32_e32 v231, 16, v231
	v_mul_f32_e32 v18, v232, v231
	v_mul_f32_e32 v231, v233, v231
	v_fma_f32 v233, v233, v230, -v18
	v_fmac_f32_e32 v231, v232, v230
	v_bfe_u32 v230, v233, 16, 1
	v_bfe_u32 v232, v231, 16, 1
	v_add3_u32 v233, v233, v230, s10
	v_add3_u32 v230, v231, v232, s10
	global_store_short_d16_hi v[202:203], v233, off
	global_store_short_d16_hi v[202:203], v230, off offset:32
	s_waitcnt vmcnt(14)
	v_lshlrev_b32_e32 v234, 16, v234
	v_lshlrev_b32_e32 v235, 16, v235
	v_mul_f32_e32 v18, v236, v235
	v_mul_f32_e32 v235, v237, v235
	v_fma_f32 v237, v237, v234, -v18
	v_fmac_f32_e32 v235, v236, v234
	v_bfe_u32 v234, v237, 16, 1
	v_bfe_u32 v236, v235, 16, 1
	v_add3_u32 v237, v237, v234, s10
	v_add3_u32 v234, v235, v236, s10
	global_store_short_d16_hi v[204:205], v237, off
	global_store_short_d16_hi v[204:205], v234, off offset:32
	s_branch .LBB0_566

; __device__ __forceinline__ unsigned f2bf(float f) { unsigned u = __builtin_bit_cast(unsigned, f); return (u + 0x7fffu + ((u >> 16) & 1u)) >> 16; }
; template <int L, bool WITH_LA> __device__ __forceinline__ void p_rope_la(const Args& a) {
;     bf16* proj = (bf16*)(a.ws + WS_PROJ);
;     const float* rope = (const float*)(a.ws + WS_ROPE);
;     const int gt = blockIdx.x * 512 + threadIdx.x, NGT = gridDim.x * 512;
;     for (int idx = gt; idx < M * 64; idx += NGT) {
;         const int i = idx & 15, hh = (idx >> 4) & 1, ts = (idx >> 5) & 1, m = idx >> 6, t = m & (T - 1);
;         bf16* p = proj + (size_t)m * PW + (ts ? PKW : PKS) + hh * 128 + i;
;         const float x1 = bf1(p[0]), x2 = bf1(p[16]), c = rope[t * 32 + i], s = rope[t * 32 + 16 + i];
;         p[0] = (bf16)f2bf(x1 * c - x2 * s); p[16] = (bf16)f2bf(x2 * c + x1 * s);
;     }
.LBB0_1509:
	v_readlane_b32 s0, v255, 0
	s_waitcnt vmcnt(0)
	v_lshlrev_b32_e32 v10, 3, v0
	v_lshl_or_b32 v3, s0, 9, v0
	s_mov_b32 s0, 0x100000
	v_cmp_gt_i32_e32 vcc, s0, v3
	s_and_saveexec_b64 s[0:1], vcc
	s_cbranch_execz .LBB0_1512
	s_add_u32 s2, s66, 0x200000
	v_and_b32_e32 v2, 15, v0
	v_mov_b32_e32 v5, 0
	v_readlane_b32 s6, v255, 0
	s_addc_u32 s3, s67, 0
	s_waitcnt lgkmcnt(0)
	s_lshl_b32 s8, s42, 9
	v_lshl_or_b32 v11, s6, 12, v10
	s_lshl_b32 s9, s42, 12
	s_mov_b64 s[6:7], 0
	s_movk_i32 s10, 0x2e00
	v_mov_b64_e32 v[6:7], s[18:19]
	v_mov_b32_e32 v12, 0x1000
	v_mov_b32_e32 v13, 0xc00
	v_lshlrev_b32_e32 v8, 1, v2
	v_mov_b32_e32 v9, v5
	s_mov_b32 s11, 0x1ffe0
	s_movk_i32 s12, 0x7fff
	s_mov_b32 s13, 0xfffff
	s_cmpk_lg_u32 s42, 0x100
	s_cbranch_scc1 .LBB0_1511
	v_and_b32_e32 v4, 32, v3
	v_ashrrev_i32_e32 v16, 6, v3
	v_cmp_eq_u32_e32 vcc, 0, v4
	v_and_b32_e32 v17, 0x80, v11
	v_mad_i64_i32 v[190:191], s[14:15], v16, s10, v[6:7]
	v_cndmask_b32_e32 v4, v12, v13, vcc
	v_lshlrev_b32_e32 v16, 5, v16
	v_lshl_add_u64 v[190:191], v[190:191], 0, v[4:5]
	v_lshlrev_b32_e32 v4, 1, v17
	v_and_or_b32 v16, v16, s11, v2
	v_lshl_add_u64 v[190:191], v[190:191], 0, v[4:5]
	v_lshlrev_b32_e32 v4, 2, v16
	v_lshl_add_u64 v[190:191], v[190:191], 0, v[8:9]
	global_load_ushort v206, v[190:191], off
	global_load_ushort v207, v[190:191], off offset:32
	global_load_dword v208, v4, s[2:3] offset:64
	s_nop 0
	global_load_dword v209, v4, s[2:3]
	v_add_u32_e32 v3, s8, v3
	v_add_u32_e32 v11, s9, v11
	v_and_b32_e32 v4, 32, v3
	v_ashrrev_i32_e32 v16, 6, v3
	v_cmp_eq_u32_e32 vcc, 0, v4
	v_and_b32_e32 v17, 0x80, v11
	v_mad_i64_i32 v[192:193], s[14:15], v16, s10, v[6:7]
	v_cndmask_b32_e32 v4, v12, v13, vcc
	v_lshlrev_b32_e32 v16, 5, v16
	v_lshl_add_u64 v[192:193], v[192:193], 0, v[4:5]
	v_lshlrev_b32_e32 v4, 1, v17
	v_and_or_b32 v16, v16, s11, v2
	v_lshl_add_u64 v[192:193], v[192:193], 0, v[4:5]
	v_lshlrev_b32_e32 v4, 2, v16
	v_lshl_add_u64 v[192:193], v[192:193], 0, v[8:9]
	global_load_ushort v210, v[192:193], off
	global_load_ushort v211, v[192:193], off offset:32
	global_load_dword v212, v4, s[2:3] offset:64
	s_nop 0
	global_load_dword v213, v4, s[2:3]
	v_add_u32_e32 v3, s8, v3
	v_add_u32_e32 v11, s9, v11
	v_and_b32_e32 v4, 32, v3
	v_ashrrev_i32_e32 v16, 6, v3
	v_cmp_eq_u32_e32 vcc, 0, v4
	v_and_b32_e32 v17, 0x80, v11
	v_mad_i64_i32 v[194:195], s[14:15], v16, s10, v[6:7]
	v_cndmask_b32_e32 v4, v12, v13, vcc
	v_lshlrev_b32_e32 v16, 5, v16
	v_lshl_add_u64 v[194:195], v[194:195], 0, v[4:5]
	v_lshlrev_b32_e32 v4, 1, v17
	v_and_or_b32 v16, v16, s11, v2
	v_lshl_add_u64 v[194:195], v[194:195], 0, v[4:5]
	v_lshlrev_b32_e32 v4, 2, v16
	v_lshl_add_u64 v[194:195], v[194:195], 0, v[8:9]
	global_load_ushort v214, v[194:195], off
	global_load_ushort v215, v[194:195], off offset:32
	global_load_dword v216, v4, s[2:3] offset:64
	s_nop 0
	global_load_dword v217, v4, s[2:3]
	v_add_u32_e32 v3, s8, v3
	v_add_u32_e32 v11, s9, v11
	v_and_b32_e32 v4, 32, v3
	v_ashrrev_i32_e32 v16, 6, v3
	v_cmp_eq_u32_e32 vcc, 0, v4
	v_and_b32_e32 v17, 0x80, v11
	v_mad_i64_i32 v[196:197], s[14:15], v16, s10, v[6:7]
	v_cndmask_b32_e32 v4, v12, v13, vcc
	v_lshlrev_b32_e32 v16, 5, v16
	v_lshl_add_u64 v[196:197], v[196:197], 0, v[4:5]
	v_lshlrev_b32_e32 v4, 1, v17
	v_and_or_b32 v16, v16, s11, v2
	v_lshl_add_u64 v[196:197], v[196:197], 0, v[4:5]
	v_lshlrev_b32_e32 v4, 2, v16
	v_lshl_add_u64 v[196:197], v[196:197], 0, v[8:9]
	global_load_ushort v218, v[196:197], off
	global_load_ushort v219, v[196:197], off offset:32
	global_load_dword v220, v4, s[2:3] offset:64
	s_nop 0
	global_load_dword v221, v4, s[2:3]
	v_add_u32_e32 v3, s8, v3
	v_add_u32_e32 v11, s9, v11
	v_and_b32_e32 v4, 32, v3
	v_ashrrev_i32_e32 v16, 6, v3
	v_cmp_eq_u32_e32 vcc, 0, v4
	v_and_b32_e32 v17, 0x80, v11
	v_mad_i64_i32 v[198:199], s[14:15], v16, s10, v[6:7]
	v_cndmask_b32_e32 v4, v12, v13, vcc
	v_lshlrev_b32_e32 v16, 5, v16
	v_lshl_add_u64 v[198:199], v[198:199], 0, v[4:5]
	v_lshlrev_b32_e32 v4, 1, v17
	v_and_or_b32 v16, v16, s11, v2
	v_lshl_add_u64 v[198:199], v[198:199], 0, v[4:5]
	v_lshlrev_b32_e32 v4, 2, v16
	v_lshl_add_u64 v[198:199], v[198:199], 0, v[8:9]
	global_load_ushort v222, v[198:199], off
	global_load_ushort v223, v[198:199], off offset:32
	global_load_dword v224, v4, s[2:3] offset:64
	s_nop 0
	global_load_dword v225, v4, s[2:3]
	v_add_u32_e32 v3, s8, v3
	v_add_u32_e32 v11, s9, v11
	v_and_b32_e32 v4, 32, v3
	v_ashrrev_i32_e32 v16, 6, v3
	v_cmp_eq_u32_e32 vcc, 0, v4
	v_and_b32_e32 v17, 0x80, v11
	v_mad_i64_i32 v[200:201], s[14:15], v16, s10, v[6:7]
	v_cndmask_b32_e32 v4, v12, v13, vcc
	v_lshlrev_b32_e32 v16, 5, v16
	v_lshl_add_u64 v[200:201], v[200:201], 0, v[4:5]
	v_lshlrev_b32_e32 v4, 1, v17
	v_and_or_b32 v16, v16, s11, v2
	v_lshl_add_u64 v[200:201], v[200:201], 0, v[4:5]
	v_lshlrev_b32_e32 v4, 2, v16
	v_lshl_add_u64 v[200:201], v[200:201], 0, v[8:9]
	global_load_ushort v226, v[200:201], off
	global_load_ushort v227, v[200:201], off offset:32
	global_load_dword v228, v4, s[2:3] offset:64
	s_nop 0
	global_load_dword v229, v4, s[2:3]
	v_add_u32_e32 v3, s8, v3
	v_add_u32_e32 v11, s9, v11
	v_and_b32_e32 v4, 32, v3
	v_ashrrev_i32_e32 v16, 6, v3
	v_cmp_eq_u32_e32 vcc, 0, v4
	v_and_b32_e32 v17, 0x80, v11
	v_mad_i64_i32 v[202:203], s[14:15], v16, s10, v[6:7]
	v_cndmask_b32_e32 v4, v12, v13, vcc
	v_lshlrev_b32_e32 v16, 5, v16
	v_lshl_add_u64 v[202:203], v[202:203], 0, v[4:5]
	v_lshlrev_b32_e32 v4, 1, v17
	v_and_or_b32 v16, v16, s11, v2
	v_lshl_add_u64 v[202:203], v[202:203], 0, v[4:5]
	v_lshlrev_b32_e32 v4, 2, v16
	v_lshl_add_u64 v[202:203], v[202:203], 0, v[8:9]
	global_load_ushort v230, v[202:203], off
	global_load_ushort v231, v[202:203], off offset:32
	global_load_dword v232, v4, s[2:3] offset:64
	s_nop 0
	global_load_dword v233, v4, s[2:3]
	v_add_u32_e32 v3, s8, v3
	v_add_u32_e32 v11, s9, v11
	v_and_b32_e32 v4, 32, v3
	v_ashrrev_i32_e32 v16, 6, v3
	v_cmp_eq_u32_e32 vcc, 0, v4
	v_and_b32_e32 v17, 0x80, v11
	v_mad_i64_i32 v[204:205], s[14:15], v16, s10, v[6:7]
	v_cndmask_b32_e32 v4, v12, v13, vcc
	v_lshlrev_b32_e32 v16, 5, v16
	v_lshl_add_u64 v[204:205], v[204:205], 0, v[4:5]
	v_lshlrev_b32_e32 v4, 1, v17
	v_and_or_b32 v16, v16, s11, v2
	v_lshl_add_u64 v[204:205], v[204:205], 0, v[4:5]
	v_lshlrev_b32_e32 v4, 2, v16
	v_lshl_add_u64 v[204:205], v[204:205], 0, v[8:9]
	global_load_ushort v234, v[204:205], off
	global_load_ushort v235, v[204:205], off offset:32
	global_load_dword v236, v4, s[2:3] offset:64
	s_nop 0
	global_load_dword v237, v4, s[2:3]
	v_add_u32_e32 v3, s8, v3
	v_add_u32_e32 v11, s9, v11
	s_waitcnt vmcnt(28)
; __device__ __forceinline__ unsigned f2bf(float f) { unsigned u = __builtin_bit_cast(unsigned, f); return (u + 0x7fffu + ((u >> 16) & 1u)) >> 16; }
; template <int L, bool WITH_LA> __device__ __forceinline__ void p_rope_la(const Args& a) {
;     ...
;     for (int idx = gt; idx < M * 64; idx += NGT) {
;         const int i = idx & 15, hh = (idx >> 4) & 1, ts = (idx >> 5) & 1, m = idx >> 6, t = m & (T - 1);
;         bf16* p = proj + (size_t)m * PW + (ts ? PKW : PKS) + hh * 128 + i;
;         const float x1 = bf1(p[0]), x2 = bf1(p[16]), c = rope[t * 32 + i], s = rope[t * 32 + 16 + i];
;         p[0] = (bf16)f2bf(x1 * c - x2 * s); p[16] = (bf16)f2bf(x2 * c + x1 * s);
;     }
	v_lshlrev_b32_e32 v206, 16, v206
	v_lshlrev_b32_e32 v207, 16, v207
	v_mul_f32_e32 v19, v208, v207
	v_mul_f32_e32 v207, v209, v207
	v_fma_f32 v209, v209, v206, -v19
	v_fmac_f32_e32 v207, v208, v206
	v_bfe_u32 v206, v209, 16, 1
	v_bfe_u32 v208, v207, 16, 1
	v_add3_u32 v209, v209, v206, s12
	v_add3_u32 v206, v207, v208, s12
	global_store_short_d16_hi v[190:191], v209, off
	global_store_short_d16_hi v[190:191], v206, off offset:32
	s_waitcnt vmcnt(26)
	v_lshlrev_b32_e32 v210, 16, v210
	v_lshlrev_b32_e32 v211, 16, v211
	v_mul_f32_e32 v19, v212, v211
	v_mul_f32_e32 v211, v213, v211
	v_fma_f32 v213, v213, v210, -v19
	v_fmac_f32_e32 v211, v212, v210
	v_bfe_u32 v210, v213, 16, 1
	v_bfe_u32 v212, v211, 16, 1
	v_add3_u32 v213, v213, v210, s12
	v_add3_u32 v210, v211, v212, s12
	global_store_short_d16_hi v[192:193], v213, off
	global_store_short_d16_hi v[192:193], v210, off offset:32
	s_waitcnt vmcnt(24)
	v_lshlrev_b32_e32 v214, 16, v214
	v_lshlrev_b32_e32 v215, 16, v215
	v_mul_f32_e32 v19, v216, v215
	v_mul_f32_e32 v215, v217, v215
	v_fma_f32 v217, v217, v214, -v19
	v_fmac_f32_e32 v215, v216, v214
	v_bfe_u32 v214, v217, 16, 1
	v_bfe_u32 v216, v215, 16, 1
	v_add3_u32 v217, v217, v214, s12
	v_add3_u32 v214, v215, v216, s12
	global_store_short_d16_hi v[194:195], v217, off
	global_store_short_d16_hi v[194:195], v214, off offset:32
	s_waitcnt vmcnt(22)
	v_lshlrev_b32_e32 v218, 16, v218
	v_lshlrev_b32_e32 v219, 16, v219
	v_mul_f32_e32 v19, v220, v219
	v_mul_f32_e32 v219, v221, v219
	v_fma_f32 v221, v221, v218, -v19
	v_fmac_f32_e32 v219, v220, v218
	v_bfe_u32 v218, v221, 16, 1
	v_bfe_u32 v220, v219, 16, 1
	v_add3_u32 v221, v221, v218, s12
	v_add3_u32 v218, v219, v220, s12
	global_store_short_d16_hi v[196:197], v221, off
	global_store_short_d16_hi v[196:197], v218, off offset:32
	s_waitcnt vmcnt(20)
	v_lshlrev_b32_e32 v222, 16, v222
	v_lshlrev_b32_e32 v223, 16, v223
	v_mul_f32_e32 v19, v224, v223
	v_mul_f32_e32 v223, v225, v223
	v_fma_f32 v225, v225, v222, -v19
	v_fmac_f32_e32 v223, v224, v222
	v_bfe_u32 v222, v225, 16, 1
	v_bfe_u32 v224, v223, 16, 1
	v_add3_u32 v225, v225, v222, s12
	v_add3_u32 v222, v223, v224, s12
	global_store_short_d16_hi v[198:199], v225, off
	global_store_short_d16_hi v[198:199], v222, off offset:32
	s_waitcnt vmcnt(18)
	v_lshlrev_b32_e32 v226, 16, v226
	v_lshlrev_b32_e32 v227, 16, v227
	v_mul_f32_e32 v19, v228, v227
	v_mul_f32_e32 v227, v229, v227
	v_fma_f32 v229, v229, v226, -v19
	v_fmac_f32_e32 v227, v228, v226
	v_bfe_u32 v226, v229, 16, 1
	v_bfe_u32 v228, v227, 16, 1
	v_add3_u32 v229, v229, v226, s12
	v_add3_u32 v226, v227, v228, s12
	global_store_short_d16_hi v[200:201], v229, off
	global_store_short_d16_hi v[200:201], v226, off offset:32
	s_waitcnt vmcnt(16)
	v_lshlrev_b32_e32 v230, 16, v230
	v_lshlrev_b32_e32 v231, 16, v231
	v_mul_f32_e32 v19, v232, v231
	v_mul_f32_e32 v231, v233, v231
	v_fma_f32 v233, v233, v230, -v19
	v_fmac_f32_e32 v231, v232, v230
	v_bfe_u32 v230, v233, 16, 1
	v_bfe_u32 v232, v231, 16, 1
	v_add3_u32 v233, v233, v230, s12
	v_add3_u32 v230, v231, v232, s12
	global_store_short_d16_hi v[202:203], v233, off
	global_store_short_d16_hi v[202:203], v230, off offset:32
	s_waitcnt vmcnt(14)
	v_lshlrev_b32_e32 v234, 16, v234
	v_lshlrev_b32_e32 v235, 16, v235
	v_mul_f32_e32 v19, v236, v235
	v_mul_f32_e32 v235, v237, v235
	v_fma_f32 v237, v237, v234, -v19
	v_fmac_f32_e32 v235, v236, v234
	v_bfe_u32 v234, v237, 16, 1
	v_bfe_u32 v236, v235, 16, 1
	v_add3_u32 v237, v237, v234, s12
	v_add3_u32 v234, v235, v236, s12
	global_store_short_d16_hi v[204:205], v237, off
	global_store_short_d16_hi v[204:205], v234, off offset:32
	s_branch .LBB0_1512
